# baseline (speedup 1.0000x reference)
.LBB0_23:
	s_andn2_b64 vcc, exec, s[4:5]
	s_cbranch_vccnz .LBB0_43
	s_load_dwordx2 s[4:5], s[0:1], 0x0
	s_add_i32 s3, s2, 0xfffffdd6
	s_ashr_i32 s76, s3, 4
	v_lshlrev_b32_e32 v43, 3, v31
	v_lshl_or_b32 v2, s76, 5, v43
	v_lshrrev_b32_e32 v42, 8, v0
	s_lshl_b32 s3, s3, 1
	v_ashrrev_i32_e32 v3, 31, v2
	v_and_or_b32 v1, s3, 30, v42
	v_lshlrev_b64 v[2:3], 15, v[2:3]
	s_waitcnt lgkmcnt(0)
	v_lshl_add_u64 v[2:3], s[4:5], 0, v[2:3]
	v_lshlrev_b32_e32 v38, 10, v1
	v_mov_b32_e32 v39, 0
	v_lshl_add_u64 v[2:3], v[2:3], 0, v[38:39]
	v_lshlrev_b32_e32 v38, 4, v30
	v_lshl_add_u64 v[2:3], v[2:3], 0, v[38:39]
	s_mov_b32 s3, 0x8000
	v_add_co_u32_e32 v4, vcc, s3, v2
	s_mov_b32 s3, 0x10000
	s_nop 0
	v_addc_co_u32_e32 v5, vcc, 0, v3, vcc
	global_load_dwordx4 v[34:37], v[2:3], off sc0 nt
	global_load_dwordx4 v[26:29], v[4:5], off sc0 nt
	v_add_co_u32_e32 v4, vcc, s3, v2
	s_mov_b32 s3, 0x18000
	s_nop 0
	v_addc_co_u32_e32 v5, vcc, 0, v3, vcc
	v_add_co_u32_e32 v6, vcc, s3, v2
	s_mov_b32 s3, 0x20000
	s_nop 0
	v_addc_co_u32_e32 v7, vcc, 0, v3, vcc
	global_load_dwordx4 v[22:25], v[4:5], off sc0 nt
	global_load_dwordx4 v[18:21], v[6:7], off sc0 nt
	v_add_co_u32_e32 v4, vcc, s3, v2
	s_mov_b32 s3, 0x28000
	s_nop 0
	v_addc_co_u32_e32 v5, vcc, 0, v3, vcc
	v_add_co_u32_e32 v6, vcc, s3, v2
	s_mov_b32 s3, 0x30000
	s_nop 0
	v_addc_co_u32_e32 v7, vcc, 0, v3, vcc
	v_add_co_u32_e32 v32, vcc, s3, v2
	s_mov_b32 s3, 0x38000
	s_nop 0
	v_addc_co_u32_e32 v33, vcc, 0, v3, vcc
	v_add_co_u32_e32 v40, vcc, s3, v2
	global_load_dwordx4 v[14:17], v[4:5], off sc0 nt
	global_load_dwordx4 v[10:13], v[6:7], off sc0 nt
	v_addc_co_u32_e32 v41, vcc, 0, v3, vcc
	global_load_dwordx4 v[6:9], v[32:33], off sc0 nt
	global_load_dwordx4 v[2:5], v[40:41], off sc0 nt
	v_mbcnt_lo_u32_b32 v33, -1, 0
	v_mbcnt_hi_u32_b32 v33, -1, v33
	v_and_b32_e32 v40, 64, v33
	v_xor_b32_e32 v39, 1, v33
	v_add_u32_e32 v40, 64, v40
	v_cmp_lt_i32_e32 vcc, v39, v40
	v_mov_b32_e32 v32, 0x800
	v_lshl_or_b32 v32, v42, 10, v32
	v_cndmask_b32_e32 v33, v33, v39, vcc
	v_lshlrev_b32_e32 v33, 2, v33
	s_waitcnt vmcnt(7)
	v_cmp_neq_f32_e32 vcc, 0, v34
	s_nop 1
	v_cndmask_b32_e64 v34, 0, 1, vcc
	v_cmp_neq_f32_e32 vcc, 0, v35
	s_nop 1
	v_cndmask_b32_e64 v35, 0, 2, vcc
	v_cmp_neq_f32_e32 vcc, 0, v36
	v_or_b32_e32 v34, v35, v34
	s_nop 0
	v_cndmask_b32_e64 v36, 0, 4, vcc
	v_cmp_neq_f32_e32 vcc, 0, v37
	s_nop 1
	v_cndmask_b32_e64 v35, 0, 8, vcc
	v_or3_b32 v35, v34, v36, v35
	ds_bpermute_b32 v36, v33, v35
	v_and_b32_e32 v34, 1, v0
	v_cmp_eq_u32_e32 vcc, 0, v34
	v_or_b32_e32 v34, v32, v43
	v_add_u32_e32 v34, v34, v38
	s_and_saveexec_b64 s[4:5], vcc
	s_cbranch_execz .LBB0_26
	s_waitcnt lgkmcnt(0)
	v_lshl_or_b32 v35, v36, 4, v35
	ds_write_b8 v34, v35
